# P4 retention-output loop: q / S-state fragment loads issued before the unit barrier and K/V waits (prologue de-serialisation), waits +16
# baseline (speedup 1.0000x reference)
; #define GAS __attribute__((address_space(1)))
; #define MFMA32(a, b, c) __builtin_amdgcn_mfma_f32_32x32x16_bf16((a), (b), (c), 0, 0, 0)
; DI void ret_out_phase(LAS unsigned char* lds, const bf16* PROJ, bf16* MIX, const bf16* ST, const float* gret, int bx, int G, int tid) {
;     ...
;     for (int unit = bx; unit < 2048; unit += G) {
;         const int n = unit & 63, hd = (unit >> 6) & 15, b = unit >> 10;
;         const size_t m0 = (size_t)b * SEQ + 128 * n, qrow = m0 + 32 * qg + r;
;         __syncthreads();
;         tile_st(KT, KSTR, kreg, tid); tile_st(VT, VSTR, vreg, tid);
;         bf16x8 qf[8]; load_qf(qf, PROJ + qrow * INW + C_RQ + 128 * hd, h);
;         const bf16* st = ST + (size_t)unit * 16384;
;         f32x16 O[2];
; #pragma unroll
;         for (int et = 0; et < 2; ++et) {
;             bf16x8 sa[8];
; #pragma unroll
;             for (int ks = 0; ks < 8; ++ks) sa[ks] = *(const GAS bf16x8*)(st + (32 * (2 * eh + et) + r) * 128 + 16 * ks + 8 * h);
; #pragma unroll
;             for (int i = 0; i < 16; ++i) O[et][i] = 0.f;
; #pragma unroll
;             for (int ks = 0; ks < 8; ++ks) O[et] = MFMA32(sa[ks], qf[ks], O[et]);
;         }
;         const float g1 = __builtin_amdgcn_exp2f(1.4426950408889634f * LOGG[hd]);
; #pragma unroll
;         for (int et = 0; et < 2; ++et) O[et] = O[et] * g1;
;         const bf16* grow = PROJ + qrow * INW + C_RG + 128 * hd;
;         v2u gt[2][4]; f32x4 gg[2][4];
; #pragma unroll
;         for (int et = 0; et < 2; ++et)
; #pragma unroll
;             for (int Gq = 0; Gq < 4; ++Gq) { const int e = 32 * (2 * eh + et) + 8 * Gq + 4 * h; gt[et][Gq] = *(const GAS v2u*)(grow + e); gg[et][Gq] = *(const f32x4*)(gret + e); }
;         __syncthreads();
;         if (unit + G < 2048) { const int u2 = unit + G, n2 = u2 & 63, hd2 = (u2 >> 6) & 15, b2 = u2 >> 10; const size_t m2 = (size_t)b2 * SEQ + 128 * n2;
;             tile_ld(kreg, PROJ + m2 * INW + C_RK + 128 * hd2, INW, tid); tile_ld(vreg, PROJ + m2 * INW + C_RV + 128 * hd2, INW, tid); }
;         for (int kt = 0; kt <= qg; ++kt) {
.LBB0_549:
	s_ashr_i32 s4, s96, 10
	s_ashr_i32 s5, s4, 31
	s_lshl_b32 s40, s96, 7
	s_lshl_b64 s[4:5], s[4:5], 13
	s_and_b32 s40, s40, 0x1f80
	s_or_b32 s4, s4, s40
	v_or_b32_e32 v168, s4, v148
	v_mov_b64_e32 v[2:3], s[42:43]
	s_movk_i32 s4, 0x7000
	s_bfe_u32 s93, s96, 0x40006
	v_mad_u64_u32 v[2:3], s[52:53], v168, s4, v[2:3]
	s_ashr_i32 s97, s96, 31
	v_mad_i32_i24 v3, s5, v202, v3
	s_lshl_b32 s40, s93, 8
	s_lshl_b64 s[4:5], s[96:97], 15
	v_lshl_add_u64 v[18:19], v[2:3], 0, s[40:41]
	v_lshlrev_b32_e32 v146, 1, v170
	v_lshl_add_u64 v[48:49], v[150:151], 0, s[4:5]
	v_lshl_add_u64 v[2:3], v[18:19], 0, v[146:147]
	v_lshl_add_u64 v[6:7], v[152:153], 1, v[48:49]
	global_load_dwordx4 v[138:141], v[2:3], off
	global_load_dwordx4 v[130:133], v[2:3], off offset:32
	global_load_dwordx4 v[126:129], v[2:3], off offset:64
	global_load_dwordx4 v[122:125], v[2:3], off offset:96
	global_load_dwordx4 v[118:121], v[2:3], off offset:128
	global_load_dwordx4 v[114:117], v[2:3], off offset:160
	global_load_dwordx4 v[106:109], v[2:3], off offset:192
	global_load_dwordx4 v[90:93], v[2:3], off offset:224
	s_nop 0
	global_load_dwordx4 v[2:5], v[6:7], off
	global_load_dwordx4 v[20:23], v[6:7], off offset:32
	global_load_dwordx4 v[24:27], v[6:7], off offset:64
	global_load_dwordx4 v[28:31], v[6:7], off offset:96
	global_load_dwordx4 v[32:35], v[6:7], off offset:128
	global_load_dwordx4 v[36:39], v[6:7], off offset:160
	global_load_dwordx4 v[40:43], v[6:7], off offset:192
	global_load_dwordx4 v[44:47], v[6:7], off offset:224
	s_waitcnt lgkmcnt(0)
	s_barrier
	s_waitcnt vmcnt(23)
	ds_write_b128 v195, v[50:53]
	s_waitcnt vmcnt(22)
	ds_write_b128 v196, v[54:57]
	s_waitcnt vmcnt(21)
	ds_write_b128 v195, v[58:61] offset:17408
	s_waitcnt vmcnt(20)
	ds_write_b128 v197, v[62:65]
	s_waitcnt vmcnt(19)
	ds_write_b128 v198, v[66:69] offset:40960
	s_waitcnt vmcnt(18)
	ds_write_b128 v199, v[70:73] offset:40960
	s_waitcnt vmcnt(17)
	ds_write_b128 v198, v[74:77] offset:61440
	s_waitcnt vmcnt(16)
	ds_write_b128 v200, v[78:81] offset:40960
	s_movk_i32 s4, 0x2000
	v_mov_b32_e32 v159, v147
	v_lshl_add_u64 v[18:19], v[18:19], 0, v[158:159]
	s_add_i32 s96, s96, s80
	s_cmpk_gt_i32 s96, 0x7ff
	s_waitcnt vmcnt(7)
	v_mfma_f32_32x32x16_bf16 v[2:17], v[2:5], v[138:141], 0
	s_waitcnt vmcnt(6)
	v_mfma_f32_32x32x16_bf16 v[2:17], v[20:23], v[130:133], v[2:17]
	v_lshl_add_u64 v[20:21], v[154:155], 1, v[48:49]
	s_waitcnt vmcnt(5)
	v_mfma_f32_32x32x16_bf16 v[2:17], v[24:27], v[126:129], v[2:17]
	s_waitcnt vmcnt(4)
	v_mfma_f32_32x32x16_bf16 v[2:17], v[28:31], v[122:125], v[2:17]
	s_waitcnt vmcnt(3)
	v_mfma_f32_32x32x16_bf16 v[2:17], v[32:35], v[118:121], v[2:17]
	v_add_co_u32_e32 v32, vcc, s4, v20
	s_mov_b64 s[4:5], 0x4000
	s_nop 0
	v_addc_co_u32_e32 v33, vcc, 0, v21, vcc
	global_load_dwordx4 v[20:23], v[32:33], off
	global_load_dwordx4 v[24:27], v[32:33], off offset:32
	global_load_dwordx4 v[28:31], v[32:33], off offset:64
	global_load_dwordx4 v[82:85], v[32:33], off offset:96
	global_load_dwordx4 v[86:89], v[32:33], off offset:128
	global_load_dwordx4 v[94:97], v[32:33], off offset:160
	global_load_dwordx4 v[98:101], v[32:33], off offset:192
	global_load_dwordx4 v[102:105], v[32:33], off offset:224
	s_waitcnt vmcnt(10)
	v_mfma_f32_32x32x16_bf16 v[2:17], v[36:39], v[114:117], v[2:17]
	s_waitcnt vmcnt(9)
	v_mfma_f32_32x32x16_bf16 v[2:17], v[40:43], v[106:109], v[2:17]
	s_waitcnt vmcnt(8)
	v_mfma_f32_32x32x16_bf16 v[2:17], v[44:47], v[90:93], v[2:17]
	s_waitcnt vmcnt(7)
	v_mfma_f32_32x32x16_bf16 v[34:49], v[20:23], v[138:141], 0
	v_lshl_add_u64 v[20:21], v[18:19], 0, s[4:5]
	s_movk_i32 s4, 0x4000
	v_add_co_u32_e32 v18, vcc, s4, v18
	s_cselect_b64 s[4:5], -1, 0
	s_nop 0
	v_addc_co_u32_e32 v19, vcc, 0, v19, vcc
	s_waitcnt vmcnt(6)
	v_mfma_f32_32x32x16_bf16 v[34:49], v[24:27], v[130:133], v[34:49]
	s_and_b64 vcc, exec, s[4:5]
	s_waitcnt vmcnt(5)
	v_mfma_f32_32x32x16_bf16 v[34:49], v[28:31], v[126:129], v[34:49]
	s_waitcnt vmcnt(4)
	v_mfma_f32_32x32x16_bf16 v[34:49], v[82:85], v[122:125], v[34:49]
	s_waitcnt vmcnt(3)
	v_mfma_f32_32x32x16_bf16 v[34:49], v[86:89], v[118:121], v[34:49]
	s_waitcnt vmcnt(2)
	v_mfma_f32_32x32x16_bf16 v[34:49], v[94:97], v[114:117], v[34:49]
	s_waitcnt vmcnt(1)
	v_mfma_f32_32x32x16_bf16 v[34:49], v[98:101], v[106:109], v[34:49]
	s_waitcnt vmcnt(0)
	v_mfma_f32_32x32x16_bf16 v[34:49], v[102:105], v[90:93], v[34:49]
	global_load_dwordx2 v[186:187], v[18:19], off
	global_load_dwordx4 v[142:145], v[156:157], off
	global_load_dwordx2 v[184:185], v[20:21], off offset:16
	global_load_dwordx4 v[134:137], v[156:157], off offset:32
	global_load_dwordx2 v[182:183], v[20:21], off offset:32
	global_load_dwordx4 v[110:113], v[156:157], off offset:64
	global_load_dwordx2 v[180:181], v[20:21], off offset:48
	global_load_dwordx4 v[102:105], v[156:157], off offset:96
	global_load_dwordx2 v[178:179], v[20:21], off offset:64
	global_load_dwordx4 v[98:101], v[156:157], off offset:128
	global_load_dwordx2 v[176:177], v[20:21], off offset:80
	global_load_dwordx4 v[94:97], v[156:157], off offset:160
	global_load_dwordx2 v[174:175], v[20:21], off offset:96
	global_load_dwordx4 v[86:89], v[156:157], off offset:192
	global_load_dwordx2 v[172:173], v[20:21], off offset:112
	global_load_dwordx4 v[82:85], v[156:157], off offset:224
	s_waitcnt lgkmcnt(0)
	s_barrier
	s_cbranch_vccnz .LBB0_551
	s_ashr_i32 s52, s96, 10
	s_ashr_i32 s53, s52, 31
	s_lshl_b32 s40, s96, 7
	s_lshl_b64 s[52:53], s[52:53], 13
	s_and_b32 s40, s40, 0x1f80
	s_or_b32 s40, s52, s40
	s_mul_i32 s52, s53, 0x7000
	s_mul_hi_u32 s53, s40, 0x7000
	s_add_i32 s53, s53, s52
	s_mulk_i32 s40, 0x7000
	s_add_u32 s40, s42, s40
	s_addc_u32 s53, s43, s53
	s_lshl_b32 s52, s96, 2
	s_and_b32 s52, s52, 0xf00
	s_add_u32 s52, s40, s52
	v_mov_b32_e32 v161, v147
	s_addc_u32 s53, s53, 0
	v_lshl_add_u64 v[18:19], s[52:53], 0, v[160:161]
	v_lshl_add_u64 v[20:21], v[18:19], 0, s[50:51]
	v_mov_b32_e32 v163, v147
	v_lshl_add_u64 v[22:23], v[20:21], 0, v[162:163]
	v_mov_b32_e32 v165, v147
	v_lshl_add_u64 v[24:25], v[20:21], 0, v[164:165]
	global_load_dwordx4 v[50:53], v[22:23], off
	global_load_dwordx4 v[54:57], v[24:25], off
	v_add_co_u32_e32 v22, vcc, s46, v22
	v_mov_b32_e32 v167, v147
	s_nop 0
	v_addc_co_u32_e32 v23, vcc, 0, v23, vcc
	v_lshl_add_u64 v[20:21], v[20:21], 0, v[166:167]
	v_lshl_add_u64 v[18:19], v[18:19], 0, s[90:91]
	global_load_dwordx4 v[58:61], v[22:23], off
	global_load_dwordx4 v[62:65], v[20:21], off
	v_lshl_add_u64 v[20:21], v[18:19], 0, v[162:163]
	v_lshl_add_u64 v[22:23], v[18:19], 0, v[164:165]
	global_load_dwordx4 v[66:69], v[20:21], off
	global_load_dwordx4 v[70:73], v[22:23], off
	v_add_co_u32_e32 v20, vcc, 0x1c0000, v20
	v_lshl_add_u64 v[18:19], v[18:19], 0, v[166:167]
	s_nop 0
	v_addc_co_u32_e32 v21, vcc, 0, v21, vcc
	global_load_dwordx4 v[74:77], v[20:21], off
	global_load_dwordx4 v[78:81], v[18:19], off
